# ret_out: the 16 Q/K tile-fill loads of a thread issued together (counted vmcnt) instead of 16 dependent round trips per unit
# speedup vs baseline: 1.0430x; 1.0043x over previous
.LBB0_2125:
	v_ashrrev_i32_e32 v18, 5, v3
	v_add_u32_e32 v6, s20, v18
	v_mov_b64_e32 v[4:5], s[76:77]
	s_mov_b32 s36, 0x60000
	v_mad_i64_i32 v[4:5], vcc, v6, s15, v[4:5]
	v_lshlrev_b32_e32 v6, 1, v2
	s_mov_b32 s37, 0
	v_lshl_add_u64 v[4:5], v[4:5], 0, s[80:81]
	v_and_b32_e32 v50, 0x1f0, v6
	s_movk_i32 s38, 0x800
	s_mov_b32 s39, 0
	v_lshl_add_u64 v[10:11], v[4:5], 0, v[50:51]
	v_lshl_add_u64 v[10:11], v[10:11], 0, s[38:39]
	global_load_dwordx4 v[184:187], v[10:11], off offset:-2048
	global_load_dwordx4 v[216:219], v[10:11], off offset:2048
	v_lshl_add_u64 v[10:11], v[10:11], 0, s[36:37]
	global_load_dwordx4 v[188:191], v[10:11], off offset:-2048
	global_load_dwordx4 v[220:223], v[10:11], off offset:2048
	v_lshl_add_u64 v[10:11], v[10:11], 0, s[36:37]
	global_load_dwordx4 v[192:195], v[10:11], off offset:-2048
	global_load_dwordx4 v[224:227], v[10:11], off offset:2048
	v_lshl_add_u64 v[10:11], v[10:11], 0, s[36:37]
	global_load_dwordx4 v[196:199], v[10:11], off offset:-2048
	global_load_dwordx4 v[228:231], v[10:11], off offset:2048
	v_lshl_add_u64 v[10:11], v[10:11], 0, s[36:37]
	global_load_dwordx4 v[200:203], v[10:11], off offset:-2048
	global_load_dwordx4 v[232:235], v[10:11], off offset:2048
	v_lshl_add_u64 v[10:11], v[10:11], 0, s[36:37]
	global_load_dwordx4 v[204:207], v[10:11], off offset:-2048
	global_load_dwordx4 v[236:239], v[10:11], off offset:2048
	v_lshl_add_u64 v[10:11], v[10:11], 0, s[36:37]
	global_load_dwordx4 v[208:211], v[10:11], off offset:-2048
	global_load_dwordx4 v[240:243], v[10:11], off offset:2048
	v_lshl_add_u64 v[10:11], v[10:11], 0, s[36:37]
	global_load_dwordx4 v[212:215], v[10:11], off offset:-2048
	global_load_dwordx4 v[244:247], v[10:11], off offset:2048
	v_mul_lo_u32 v19, v18, s6
	v_add_u32_e32 v19, v19, v50
	v_add_u32_e32 v20, s95, v19
	v_add_u32_e32 v4, 1, v18
	v_cvt_f32_i32_e32 v4, v4
	v_mul_f32_e32 v4, v64, v4
	v_mul_f32_e32 v5, 0x3fb8aa3b, v4
	v_fma_f32 v6, v4, s13, -v5
	v_rndne_f32_e32 v7, v5
	v_fmac_f32_e32 v6, 0x32a5705f, v4
	v_sub_f32_e32 v5, v5, v7
	v_add_f32_e32 v5, v5, v6
	v_exp_f32_e32 v5, v5
	v_cvt_i32_f32_e32 v6, v7
	v_cmp_ngt_f32_e32 vcc, s93, v4
	v_ldexp_f32 v5, v5, v6
	s_nop 0
	v_cndmask_b32_e32 v5, 0, v5, vcc
	v_cmp_nlt_f32_e32 vcc, s14, v4
	s_nop 1
	v_cndmask_b32_e32 v8, v123, v5, vcc
	s_waitcnt vmcnt(15)
	v_lshlrev_b32_e32 v12, 16, v184
	v_and_b32_e32 v13, 0xffff0000, v184
	v_lshlrev_b32_e32 v4, 16, v185
	v_and_b32_e32 v5, 0xffff0000, v185
	v_pk_mul_f32 v[14:15], v[8:9], v[4:5] op_sel_hi:[0,1]
	v_lshlrev_b32_e32 v4, 16, v186
	v_and_b32_e32 v5, 0xffff0000, v186
	v_pk_mul_f32 v[16:17], v[8:9], v[4:5] op_sel_hi:[0,1]
	v_lshlrev_b32_e32 v4, 16, v187
	v_and_b32_e32 v5, 0xffff0000, v187
	v_pk_mul_f32 v[12:13], v[8:9], v[12:13] op_sel_hi:[0,1]
	v_pk_mul_f32 v[8:9], v[8:9], v[4:5] op_sel_hi:[0,1]
	v_cvt_pk_bf16_f32 v4, v12, v13
	v_cvt_pk_bf16_f32 v5, v14, v15
	v_cvt_pk_bf16_f32 v6, v16, v17
	v_cvt_pk_bf16_f32 v7, v8, v9
	ds_write_b128 v19, v[4:7]
	s_waitcnt vmcnt(14)
	ds_write_b128 v20, v[216:219]
	v_add_u32_e32 v19, 0x2100, v19
	v_add_u32_e32 v20, 0x2100, v20
	v_add_u32_e32 v4, 17, v18
	v_cvt_f32_i32_e32 v4, v4
	v_mul_f32_e32 v4, v64, v4
	v_mul_f32_e32 v5, 0x3fb8aa3b, v4
	v_fma_f32 v6, v4, s13, -v5
	v_rndne_f32_e32 v7, v5
	v_fmac_f32_e32 v6, 0x32a5705f, v4
	v_sub_f32_e32 v5, v5, v7
	v_add_f32_e32 v5, v5, v6
	v_exp_f32_e32 v5, v5
	v_cvt_i32_f32_e32 v6, v7
	v_cmp_ngt_f32_e32 vcc, s93, v4
	v_ldexp_f32 v5, v5, v6
	s_nop 0
	v_cndmask_b32_e32 v5, 0, v5, vcc
	v_cmp_nlt_f32_e32 vcc, s14, v4
	s_nop 1
	v_cndmask_b32_e32 v8, v123, v5, vcc
	s_waitcnt vmcnt(13)
	v_lshlrev_b32_e32 v12, 16, v188
	v_and_b32_e32 v13, 0xffff0000, v188
	v_lshlrev_b32_e32 v4, 16, v189
	v_and_b32_e32 v5, 0xffff0000, v189
	v_pk_mul_f32 v[14:15], v[8:9], v[4:5] op_sel_hi:[0,1]
	v_lshlrev_b32_e32 v4, 16, v190
	v_and_b32_e32 v5, 0xffff0000, v190
	v_pk_mul_f32 v[16:17], v[8:9], v[4:5] op_sel_hi:[0,1]
	v_lshlrev_b32_e32 v4, 16, v191
	v_and_b32_e32 v5, 0xffff0000, v191
	v_pk_mul_f32 v[12:13], v[8:9], v[12:13] op_sel_hi:[0,1]
	v_pk_mul_f32 v[8:9], v[8:9], v[4:5] op_sel_hi:[0,1]
	v_cvt_pk_bf16_f32 v4, v12, v13
	v_cvt_pk_bf16_f32 v5, v14, v15
	v_cvt_pk_bf16_f32 v6, v16, v17
	v_cvt_pk_bf16_f32 v7, v8, v9
	ds_write_b128 v19, v[4:7]
	s_waitcnt vmcnt(12)
	ds_write_b128 v20, v[220:223]
	v_add_u32_e32 v19, 0x2100, v19
	v_add_u32_e32 v20, 0x2100, v20
	v_add_u32_e32 v4, 33, v18
	v_cvt_f32_i32_e32 v4, v4
	v_mul_f32_e32 v4, v64, v4
	v_mul_f32_e32 v5, 0x3fb8aa3b, v4
	v_fma_f32 v6, v4, s13, -v5
	v_rndne_f32_e32 v7, v5
	v_fmac_f32_e32 v6, 0x32a5705f, v4
	v_sub_f32_e32 v5, v5, v7
	v_add_f32_e32 v5, v5, v6
	v_exp_f32_e32 v5, v5
	v_cvt_i32_f32_e32 v6, v7
	v_cmp_ngt_f32_e32 vcc, s93, v4
	v_ldexp_f32 v5, v5, v6
	s_nop 0
	v_cndmask_b32_e32 v5, 0, v5, vcc
	v_cmp_nlt_f32_e32 vcc, s14, v4
	s_nop 1
	v_cndmask_b32_e32 v8, v123, v5, vcc
	s_waitcnt vmcnt(11)
	v_lshlrev_b32_e32 v12, 16, v192
	v_and_b32_e32 v13, 0xffff0000, v192
	v_lshlrev_b32_e32 v4, 16, v193
	v_and_b32_e32 v5, 0xffff0000, v193
	v_pk_mul_f32 v[14:15], v[8:9], v[4:5] op_sel_hi:[0,1]
	v_lshlrev_b32_e32 v4, 16, v194
	v_and_b32_e32 v5, 0xffff0000, v194
	v_pk_mul_f32 v[16:17], v[8:9], v[4:5] op_sel_hi:[0,1]
	v_lshlrev_b32_e32 v4, 16, v195
	v_and_b32_e32 v5, 0xffff0000, v195
	v_pk_mul_f32 v[12:13], v[8:9], v[12:13] op_sel_hi:[0,1]
	v_pk_mul_f32 v[8:9], v[8:9], v[4:5] op_sel_hi:[0,1]
	v_cvt_pk_bf16_f32 v4, v12, v13
	v_cvt_pk_bf16_f32 v5, v14, v15
	v_cvt_pk_bf16_f32 v6, v16, v17
	v_cvt_pk_bf16_f32 v7, v8, v9
	ds_write_b128 v19, v[4:7]
	s_waitcnt vmcnt(10)
	ds_write_b128 v20, v[224:227]
	v_add_u32_e32 v19, 0x2100, v19
	v_add_u32_e32 v20, 0x2100, v20
	v_add_u32_e32 v4, 49, v18
	v_cvt_f32_i32_e32 v4, v4
	v_mul_f32_e32 v4, v64, v4
	v_mul_f32_e32 v5, 0x3fb8aa3b, v4
	v_fma_f32 v6, v4, s13, -v5
	v_rndne_f32_e32 v7, v5
	v_fmac_f32_e32 v6, 0x32a5705f, v4
	v_sub_f32_e32 v5, v5, v7
	v_add_f32_e32 v5, v5, v6
	v_exp_f32_e32 v5, v5
	v_cvt_i32_f32_e32 v6, v7
	v_cmp_ngt_f32_e32 vcc, s93, v4
	v_ldexp_f32 v5, v5, v6
	s_nop 0
	v_cndmask_b32_e32 v5, 0, v5, vcc
	v_cmp_nlt_f32_e32 vcc, s14, v4
	s_nop 1
	v_cndmask_b32_e32 v8, v123, v5, vcc
	s_waitcnt vmcnt(9)
	v_lshlrev_b32_e32 v12, 16, v196
	v_and_b32_e32 v13, 0xffff0000, v196
	v_lshlrev_b32_e32 v4, 16, v197
	v_and_b32_e32 v5, 0xffff0000, v197
	v_pk_mul_f32 v[14:15], v[8:9], v[4:5] op_sel_hi:[0,1]
	v_lshlrev_b32_e32 v4, 16, v198
	v_and_b32_e32 v5, 0xffff0000, v198
	v_pk_mul_f32 v[16:17], v[8:9], v[4:5] op_sel_hi:[0,1]
	v_lshlrev_b32_e32 v4, 16, v199
	v_and_b32_e32 v5, 0xffff0000, v199
	v_pk_mul_f32 v[12:13], v[8:9], v[12:13] op_sel_hi:[0,1]
	v_pk_mul_f32 v[8:9], v[8:9], v[4:5] op_sel_hi:[0,1]
	v_cvt_pk_bf16_f32 v4, v12, v13
	v_cvt_pk_bf16_f32 v5, v14, v15
	v_cvt_pk_bf16_f32 v6, v16, v17
	v_cvt_pk_bf16_f32 v7, v8, v9
	ds_write_b128 v19, v[4:7]
	s_waitcnt vmcnt(8)
	ds_write_b128 v20, v[228:231]
	v_add_u32_e32 v19, 0x2100, v19
	v_add_u32_e32 v20, 0x2100, v20
	v_add_u32_e32 v4, 65, v18
	v_cvt_f32_i32_e32 v4, v4
	v_mul_f32_e32 v4, v64, v4
	v_mul_f32_e32 v5, 0x3fb8aa3b, v4
	v_fma_f32 v6, v4, s13, -v5
	v_rndne_f32_e32 v7, v5
	v_fmac_f32_e32 v6, 0x32a5705f, v4
	v_sub_f32_e32 v5, v5, v7
	v_add_f32_e32 v5, v5, v6
	v_exp_f32_e32 v5, v5
	v_cvt_i32_f32_e32 v6, v7
	v_cmp_ngt_f32_e32 vcc, s93, v4
	v_ldexp_f32 v5, v5, v6
	s_nop 0
	v_cndmask_b32_e32 v5, 0, v5, vcc
	v_cmp_nlt_f32_e32 vcc, s14, v4
	s_nop 1
	v_cndmask_b32_e32 v8, v123, v5, vcc
	s_waitcnt vmcnt(7)
	v_lshlrev_b32_e32 v12, 16, v200
	v_and_b32_e32 v13, 0xffff0000, v200
	v_lshlrev_b32_e32 v4, 16, v201
	v_and_b32_e32 v5, 0xffff0000, v201
	v_pk_mul_f32 v[14:15], v[8:9], v[4:5] op_sel_hi:[0,1]
	v_lshlrev_b32_e32 v4, 16, v202
	v_and_b32_e32 v5, 0xffff0000, v202
	v_pk_mul_f32 v[16:17], v[8:9], v[4:5] op_sel_hi:[0,1]
	v_lshlrev_b32_e32 v4, 16, v203
	v_and_b32_e32 v5, 0xffff0000, v203
	v_pk_mul_f32 v[12:13], v[8:9], v[12:13] op_sel_hi:[0,1]
	v_pk_mul_f32 v[8:9], v[8:9], v[4:5] op_sel_hi:[0,1]
	v_cvt_pk_bf16_f32 v4, v12, v13
	v_cvt_pk_bf16_f32 v5, v14, v15
	v_cvt_pk_bf16_f32 v6, v16, v17
	v_cvt_pk_bf16_f32 v7, v8, v9
	ds_write_b128 v19, v[4:7]
	s_waitcnt vmcnt(6)
	ds_write_b128 v20, v[232:235]
	v_add_u32_e32 v19, 0x2100, v19
	v_add_u32_e32 v20, 0x2100, v20
	v_add_u32_e32 v4, 81, v18
	v_cvt_f32_i32_e32 v4, v4
	v_mul_f32_e32 v4, v64, v4
	v_mul_f32_e32 v5, 0x3fb8aa3b, v4
	v_fma_f32 v6, v4, s13, -v5
	v_rndne_f32_e32 v7, v5
	v_fmac_f32_e32 v6, 0x32a5705f, v4
	v_sub_f32_e32 v5, v5, v7
	v_add_f32_e32 v5, v5, v6
	v_exp_f32_e32 v5, v5
	v_cvt_i32_f32_e32 v6, v7
	v_cmp_ngt_f32_e32 vcc, s93, v4
	v_ldexp_f32 v5, v5, v6
	s_nop 0
	v_cndmask_b32_e32 v5, 0, v5, vcc
	v_cmp_nlt_f32_e32 vcc, s14, v4
	s_nop 1
	v_cndmask_b32_e32 v8, v123, v5, vcc
	s_waitcnt vmcnt(5)
	v_lshlrev_b32_e32 v12, 16, v204
	v_and_b32_e32 v13, 0xffff0000, v204
	v_lshlrev_b32_e32 v4, 16, v205
	v_and_b32_e32 v5, 0xffff0000, v205
	v_pk_mul_f32 v[14:15], v[8:9], v[4:5] op_sel_hi:[0,1]
	v_lshlrev_b32_e32 v4, 16, v206
	v_and_b32_e32 v5, 0xffff0000, v206
	v_pk_mul_f32 v[16:17], v[8:9], v[4:5] op_sel_hi:[0,1]
	v_lshlrev_b32_e32 v4, 16, v207
	v_and_b32_e32 v5, 0xffff0000, v207
	v_pk_mul_f32 v[12:13], v[8:9], v[12:13] op_sel_hi:[0,1]
	v_pk_mul_f32 v[8:9], v[8:9], v[4:5] op_sel_hi:[0,1]
	v_cvt_pk_bf16_f32 v4, v12, v13
	v_cvt_pk_bf16_f32 v5, v14, v15
	v_cvt_pk_bf16_f32 v6, v16, v17
	v_cvt_pk_bf16_f32 v7, v8, v9
	ds_write_b128 v19, v[4:7]
	s_waitcnt vmcnt(4)
	ds_write_b128 v20, v[236:239]
	v_add_u32_e32 v19, 0x2100, v19
	v_add_u32_e32 v20, 0x2100, v20
	v_add_u32_e32 v4, 97, v18
	v_cvt_f32_i32_e32 v4, v4
	v_mul_f32_e32 v4, v64, v4
	v_mul_f32_e32 v5, 0x3fb8aa3b, v4
	v_fma_f32 v6, v4, s13, -v5
	v_rndne_f32_e32 v7, v5
	v_fmac_f32_e32 v6, 0x32a5705f, v4
	v_sub_f32_e32 v5, v5, v7
	v_add_f32_e32 v5, v5, v6
	v_exp_f32_e32 v5, v5
	v_cvt_i32_f32_e32 v6, v7
	v_cmp_ngt_f32_e32 vcc, s93, v4
	v_ldexp_f32 v5, v5, v6
	s_nop 0
	v_cndmask_b32_e32 v5, 0, v5, vcc
	v_cmp_nlt_f32_e32 vcc, s14, v4
	s_nop 1
	v_cndmask_b32_e32 v8, v123, v5, vcc
	s_waitcnt vmcnt(3)
	v_lshlrev_b32_e32 v12, 16, v208
	v_and_b32_e32 v13, 0xffff0000, v208
	v_lshlrev_b32_e32 v4, 16, v209
	v_and_b32_e32 v5, 0xffff0000, v209
	v_pk_mul_f32 v[14:15], v[8:9], v[4:5] op_sel_hi:[0,1]
	v_lshlrev_b32_e32 v4, 16, v210
	v_and_b32_e32 v5, 0xffff0000, v210
	v_pk_mul_f32 v[16:17], v[8:9], v[4:5] op_sel_hi:[0,1]
	v_lshlrev_b32_e32 v4, 16, v211
	v_and_b32_e32 v5, 0xffff0000, v211
	v_pk_mul_f32 v[12:13], v[8:9], v[12:13] op_sel_hi:[0,1]
	v_pk_mul_f32 v[8:9], v[8:9], v[4:5] op_sel_hi:[0,1]
	v_cvt_pk_bf16_f32 v4, v12, v13
	v_cvt_pk_bf16_f32 v5, v14, v15
	v_cvt_pk_bf16_f32 v6, v16, v17
	v_cvt_pk_bf16_f32 v7, v8, v9
	ds_write_b128 v19, v[4:7]
	s_waitcnt vmcnt(2)
	ds_write_b128 v20, v[240:243]
	v_add_u32_e32 v19, 0x2100, v19
	v_add_u32_e32 v20, 0x2100, v20
	v_add_u32_e32 v4, 113, v18
	v_cvt_f32_i32_e32 v4, v4
	v_mul_f32_e32 v4, v64, v4
	v_mul_f32_e32 v5, 0x3fb8aa3b, v4
	v_fma_f32 v6, v4, s13, -v5
	v_rndne_f32_e32 v7, v5
	v_fmac_f32_e32 v6, 0x32a5705f, v4
	v_sub_f32_e32 v5, v5, v7
	v_add_f32_e32 v5, v5, v6
	v_exp_f32_e32 v5, v5
	v_cvt_i32_f32_e32 v6, v7
	v_cmp_ngt_f32_e32 vcc, s93, v4
	v_ldexp_f32 v5, v5, v6
	s_nop 0
	v_cndmask_b32_e32 v5, 0, v5, vcc
	v_cmp_nlt_f32_e32 vcc, s14, v4
	s_nop 1
	v_cndmask_b32_e32 v8, v123, v5, vcc
	s_waitcnt vmcnt(1)
	v_lshlrev_b32_e32 v12, 16, v212
	v_and_b32_e32 v13, 0xffff0000, v212
	v_lshlrev_b32_e32 v4, 16, v213
	v_and_b32_e32 v5, 0xffff0000, v213
	v_pk_mul_f32 v[14:15], v[8:9], v[4:5] op_sel_hi:[0,1]
	v_lshlrev_b32_e32 v4, 16, v214
	v_and_b32_e32 v5, 0xffff0000, v214
	v_pk_mul_f32 v[16:17], v[8:9], v[4:5] op_sel_hi:[0,1]
	v_lshlrev_b32_e32 v4, 16, v215
	v_and_b32_e32 v5, 0xffff0000, v215
	v_pk_mul_f32 v[12:13], v[8:9], v[12:13] op_sel_hi:[0,1]
	v_pk_mul_f32 v[8:9], v[8:9], v[4:5] op_sel_hi:[0,1]
	v_cvt_pk_bf16_f32 v4, v12, v13
	v_cvt_pk_bf16_f32 v5, v14, v15
	v_cvt_pk_bf16_f32 v6, v16, v17
	v_cvt_pk_bf16_f32 v7, v8, v9
	ds_write_b128 v19, v[4:7]
	s_waitcnt vmcnt(0)
	ds_write_b128 v20, v[244:247]
